# conversion of layers 1-3 MoE weights inside the attention queue with a hand-written dwordx4 conversion routine, nt stores; ticket wait deferred to item end
# speedup vs baseline: 1.0395x; 1.0042x over previous
.LBB0_792:
	v_mov_b32_e32 v223, 0
	s_and_saveexec_b64 s[2:3], s[36:37]
	s_cbranch_execz .LBB0_796
	s_mov_b64 s[14:15], exec
	v_mbcnt_lo_u32_b32 v0, s14, 0
	v_mbcnt_hi_u32_b32 v0, s15, v0
	v_cmp_eq_u32_e32 vcc, 0, v0
	s_and_saveexec_b64 s[12:13], vcc
	s_cbranch_execz .LBB0_795
	s_bcnt1_i32_b64 s14, s[14:15]
	v_mov_b32_e32 v1, s14
	global_atomic_add v196, v97, v1, s[8:9] sc0
.LBB0_795:
	s_or_b64 exec, exec, s[12:13]
.LBB0_796:
	s_or_b64 exec, exec, s[2:3]
	v_readlane_b32 s101, v254, 38
	s_nop 3
	s_cmp_eq_u32 s101, 3
	s_cbranch_scc1 .Lc3_attn
	s_cmpk_lt_u32 s24, 0xe40
	s_cbranch_scc0 .Lc3_late
	s_mul_hi_u32 s101, s24, 0xaaaaaaab
	s_lshr_b32 s101, s101, 1
	s_mul_i32 s2, s101, 3
	s_sub_i32 s2, s24, s2
	s_cmp_eq_u32 s2, 2
	s_cbranch_scc1 .Lc3_entry
	s_sub_i32 s24, s24, s101
	s_branch .Lc3_chk

.LBB0_869:
	s_and_saveexec_b64 s[2:3], s[36:37]
	s_cbranch_execz .LBB0_791
	v_readlane_b32 s12, v253, 54
	s_nop 1
	v_mov_b32_e32 v0, s12
	s_waitcnt vmcnt(0)
	ds_write_b32 v0, v196
	s_branch .LBB0_791
.Lc3_entry:
	v_readlane_b32 s22, v252, 0
	v_readlane_b32 s23, v252, 1
	v_readlane_b32 s20, v254, 38
	s_lshr_b32 s2, s93, 6
	s_load_dwordx2 s[24:25], s[22:23], 0x98
	s_lshl_b32 s27, s2, 14
	s_add_i32 s20, s20, 1
	v_mbcnt_lo_u32_b32 v169, -1, 0
	v_mbcnt_hi_u32_b32 v169, -1, v169
	s_lshl_b32 s19, s101, 3
	s_add_i32 s19, s19, s2
	s_addk_i32 s19, 0xa00
	s_waitcnt lgkmcnt(0)
	s_cmpk_gt_i32 s19, 0x1fff
	v_lshrrev_b32_e32 v164, 4, v169
	v_and_b32_e32 v168, 15, v169
	v_lshrrev_b32_e32 v167, 3, v169
	s_cbranch_scc1 .Lc3_dn
	s_load_dwordx2 s[2:3], s[22:23], 0x60
	s_lshr_b32 s18, s19, 8
	s_lshl_b32 s21, s20, 5
	s_add_i32 s18, s18, s21
	s_bfe_u32 s21, s19, 0x30005
	s_and_b32 s26, s19, 31
	s_lshl_b32 s15, s18, 21
	s_add_u32 s12, s24, s15
	s_addc_u32 s13, s25, 0
	s_lshl_b32 s15, s21, 7
	s_add_i32 s15, s15, 0x3b00000
	s_lshr_b32 s14, s26, 2
	s_lshl_b32 s14, s14, 18
	s_add_i32 s15, s15, s14
	s_and_b32 s14, s26, 3
	s_lshl_b32 s14, s14, 15
	s_add_i32 s15, s15, s14
	s_add_u32 s12, s12, s15
	s_addc_u32 s13, s13, 0
	s_lshl_b32 s18, s18, 23
	s_lshl_b32 s21, s21, 20
	s_add_i32 s18, s18, s21
	s_lshl_b32 s26, s26, 8
	s_add_i32 s18, s18, s26
	s_waitcnt lgkmcnt(0)
	s_add_u32 s2, s2, s18
	s_addc_u32 s3, s3, 0
	s_movk_i32 s14, 0x2000
	s_movk_i32 s15, 0x1000
	s_mov_b32 s16, 0x42000000
	v_lshlrev_b32_e32 v164, 18, v164
	v_and_b32_e32 v166, 1, v167
	v_lshlrev_b32_e32 v166, 17, v166
	v_lshrrev_b32_e32 v167, 1, v167
	v_lshl_or_b32 v167, v167, 10, v166
	s_branch .Lc3_go
.Lc3_dn:
	s_load_dwordx2 s[2:3], s[22:23], 0x70
	s_add_i32 s26, s19, 0xffffe000
	s_lshr_b32 s18, s26, 7
	s_lshl_b32 s21, s20, 5
	s_add_i32 s18, s18, s21
	s_bfe_u32 s21, s26, 0x30004
	s_and_b32 s26, s26, 15
	s_lshl_b32 s15, s18, 20
	s_add_u32 s12, s24, s15
	s_addc_u32 s13, s25, 0
	s_lshl_b32 s15, s21, 7
	s_add_i32 s15, s15, 0x23b00000
	s_lshl_b32 s14, s26, 16
	s_add_i32 s15, s15, s14
	s_add_u32 s12, s12, s15
	s_addc_u32 s13, s13, 0
	s_lshl_b32 s18, s18, 22
	s_lshl_b32 s21, s21, 19
	s_add_i32 s18, s18, s21
	s_lshl_b32 s26, s26, 8
	s_add_i32 s18, s18, s26
	s_waitcnt lgkmcnt(0)
	s_add_u32 s2, s2, s18
	s_addc_u32 s3, s3, 0
	s_movk_i32 s14, 0x1000
	s_movk_i32 s15, 0x2000
	s_mov_b32 s16, 0x42800000
	v_lshlrev_b32_e32 v164, 17, v164
	v_lshlrev_b32_e32 v167, 10, v167
.Lc3_go:
	v_lshl_or_b32 v164, v168, 4, v164
	v_and_b32_e32 v166, 7, v169
	v_lshl_or_b32 v167, v166, 4, v167
	global_load_dwordx4 v[0:3], v164, s[2:3] nt
	s_add_u32 s2, s2, s14
	s_addc_u32 s3, s3, 0
	global_load_dwordx4 v[4:7], v164, s[2:3] nt
	s_add_u32 s2, s2, s14
	s_addc_u32 s3, s3, 0
	global_load_dwordx4 v[8:11], v164, s[2:3] nt
	s_add_u32 s2, s2, s14
	s_addc_u32 s3, s3, 0
	global_load_dwordx4 v[12:15], v164, s[2:3] nt
	s_add_u32 s2, s2, s14
	s_addc_u32 s3, s3, 0
	global_load_dwordx4 v[16:19], v164, s[2:3] nt
	s_add_u32 s2, s2, s14
	s_addc_u32 s3, s3, 0
	global_load_dwordx4 v[20:23], v164, s[2:3] nt
	s_add_u32 s2, s2, s14
	s_addc_u32 s3, s3, 0
	global_load_dwordx4 v[24:27], v164, s[2:3] nt
	s_add_u32 s2, s2, s14
	s_addc_u32 s3, s3, 0
	global_load_dwordx4 v[28:31], v164, s[2:3] nt
	s_add_u32 s2, s2, s14
	s_addc_u32 s3, s3, 0
	global_load_dwordx4 v[32:35], v164, s[2:3] nt
	s_add_u32 s2, s2, s14
	s_addc_u32 s3, s3, 0
	global_load_dwordx4 v[36:39], v164, s[2:3] nt
	s_add_u32 s2, s2, s14
	s_addc_u32 s3, s3, 0
	global_load_dwordx4 v[40:43], v164, s[2:3] nt
	s_add_u32 s2, s2, s14
	s_addc_u32 s3, s3, 0
	global_load_dwordx4 v[44:47], v164, s[2:3] nt
	s_add_u32 s2, s2, s14
	s_addc_u32 s3, s3, 0
	global_load_dwordx4 v[48:51], v164, s[2:3] nt
	s_add_u32 s2, s2, s14
	s_addc_u32 s3, s3, 0
	global_load_dwordx4 v[52:55], v164, s[2:3] nt
	s_add_u32 s2, s2, s14
	s_addc_u32 s3, s3, 0
	global_load_dwordx4 v[56:59], v164, s[2:3] nt
	s_add_u32 s2, s2, s14
	s_addc_u32 s3, s3, 0
	global_load_dwordx4 v[60:63], v164, s[2:3] nt
	s_add_u32 s2, s2, s14
	s_addc_u32 s3, s3, 0
	global_load_dwordx4 v[64:67], v164, s[2:3] nt
	s_add_u32 s2, s2, s14
	s_addc_u32 s3, s3, 0
	global_load_dwordx4 v[68:71], v164, s[2:3] nt
	s_add_u32 s2, s2, s14
	s_addc_u32 s3, s3, 0
	global_load_dwordx4 v[72:75], v164, s[2:3] nt
	s_add_u32 s2, s2, s14
	s_addc_u32 s3, s3, 0
	global_load_dwordx4 v[76:79], v164, s[2:3] nt
	s_add_u32 s2, s2, s14
	s_addc_u32 s3, s3, 0
	global_load_dwordx4 v[80:83], v164, s[2:3] nt
	s_add_u32 s2, s2, s14
	s_addc_u32 s3, s3, 0
	global_load_dwordx4 v[84:87], v164, s[2:3] nt
	s_add_u32 s2, s2, s14
	s_addc_u32 s3, s3, 0
	global_load_dwordx4 v[88:91], v164, s[2:3] nt
	s_add_u32 s2, s2, s14
	s_addc_u32 s3, s3, 0
	global_load_dwordx4 v[92:95], v164, s[2:3] nt
	s_add_u32 s2, s2, s14
	s_addc_u32 s3, s3, 0
	global_load_dwordx4 v[100:103], v164, s[2:3] nt
	s_add_u32 s2, s2, s14
	s_addc_u32 s3, s3, 0
	global_load_dwordx4 v[104:107], v164, s[2:3] nt
	s_add_u32 s2, s2, s14
	s_addc_u32 s3, s3, 0
	global_load_dwordx4 v[108:111], v164, s[2:3] nt
	s_add_u32 s2, s2, s14
	s_addc_u32 s3, s3, 0
	global_load_dwordx4 v[112:115], v164, s[2:3] nt
	s_add_u32 s2, s2, s14
	s_addc_u32 s3, s3, 0
	global_load_dwordx4 v[116:119], v164, s[2:3] nt
	s_add_u32 s2, s2, s14
	s_addc_u32 s3, s3, 0
	global_load_dwordx4 v[120:123], v164, s[2:3] nt
	s_add_u32 s2, s2, s14
	s_addc_u32 s3, s3, 0
	global_load_dwordx4 v[124:127], v164, s[2:3] nt
	s_add_u32 s2, s2, s14
	s_addc_u32 s3, s3, 0
	global_load_dwordx4 v[128:131], v164, s[2:3] nt
	v_mul_u32_u24_e32 v165, 0x240, v168
	v_lshrrev_b32_e32 v168, 4, v169
	v_lshl_add_u32 v165, v168, 5, v165
	v_add_u32_e32 v165, s27, v165
	v_lshrrev_b32_e32 v168, 3, v169
	v_mul_u32_u24_e32 v168, 0x90, v168
	v_lshl_add_u32 v166, v166, 4, v168
	v_add_u32_e32 v166, s27, v166
	s_mov_b32 s17, s16
	s_waitcnt vmcnt(28)
	v_pk_mul_f32 v[0:1], v[0:1], s[16:17] op_sel_hi:[1,0]
	v_pk_mul_f32 v[2:3], v[2:3], s[16:17] op_sel_hi:[1,0]
	v_pk_mul_f32 v[4:5], v[4:5], s[16:17] op_sel_hi:[1,0]
	v_pk_mul_f32 v[6:7], v[6:7], s[16:17] op_sel_hi:[1,0]
	v_pk_mul_f32 v[8:9], v[8:9], s[16:17] op_sel_hi:[1,0]
	v_pk_mul_f32 v[10:11], v[10:11], s[16:17] op_sel_hi:[1,0]
	v_pk_mul_f32 v[12:13], v[12:13], s[16:17] op_sel_hi:[1,0]
	v_pk_mul_f32 v[14:15], v[14:15], s[16:17] op_sel_hi:[1,0]
	v_cvt_pk_fp8_f32 v132, v0, v4
	v_cvt_pk_fp8_f32 v140, v1, v5
	v_cvt_pk_fp8_f32 v148, v2, v6
	v_cvt_pk_fp8_f32 v156, v3, v7
	v_cvt_pk_fp8_f32 v132, v8, v12 op_sel:[0,0,1]
	v_cvt_pk_fp8_f32 v140, v9, v13 op_sel:[0,0,1]
	v_cvt_pk_fp8_f32 v148, v10, v14 op_sel:[0,0,1]
	v_cvt_pk_fp8_f32 v156, v11, v15 op_sel:[0,0,1]
	s_waitcnt vmcnt(24)
	v_pk_mul_f32 v[16:17], v[16:17], s[16:17] op_sel_hi:[1,0]
	v_pk_mul_f32 v[18:19], v[18:19], s[16:17] op_sel_hi:[1,0]
	v_pk_mul_f32 v[20:21], v[20:21], s[16:17] op_sel_hi:[1,0]
	v_pk_mul_f32 v[22:23], v[22:23], s[16:17] op_sel_hi:[1,0]
	v_pk_mul_f32 v[24:25], v[24:25], s[16:17] op_sel_hi:[1,0]
	v_pk_mul_f32 v[26:27], v[26:27], s[16:17] op_sel_hi:[1,0]
	v_pk_mul_f32 v[28:29], v[28:29], s[16:17] op_sel_hi:[1,0]
	v_pk_mul_f32 v[30:31], v[30:31], s[16:17] op_sel_hi:[1,0]
	v_cvt_pk_fp8_f32 v133, v16, v20
	v_cvt_pk_fp8_f32 v141, v17, v21
	v_cvt_pk_fp8_f32 v149, v18, v22
	v_cvt_pk_fp8_f32 v157, v19, v23
	v_cvt_pk_fp8_f32 v133, v24, v28 op_sel:[0,0,1]
	v_cvt_pk_fp8_f32 v141, v25, v29 op_sel:[0,0,1]
	v_cvt_pk_fp8_f32 v149, v26, v30 op_sel:[0,0,1]
	v_cvt_pk_fp8_f32 v157, v27, v31 op_sel:[0,0,1]
	s_waitcnt vmcnt(20)
	v_pk_mul_f32 v[32:33], v[32:33], s[16:17] op_sel_hi:[1,0]
	v_pk_mul_f32 v[34:35], v[34:35], s[16:17] op_sel_hi:[1,0]
	v_pk_mul_f32 v[36:37], v[36:37], s[16:17] op_sel_hi:[1,0]
	v_pk_mul_f32 v[38:39], v[38:39], s[16:17] op_sel_hi:[1,0]
	v_pk_mul_f32 v[40:41], v[40:41], s[16:17] op_sel_hi:[1,0]
	v_pk_mul_f32 v[42:43], v[42:43], s[16:17] op_sel_hi:[1,0]
	v_pk_mul_f32 v[44:45], v[44:45], s[16:17] op_sel_hi:[1,0]
	v_pk_mul_f32 v[46:47], v[46:47], s[16:17] op_sel_hi:[1,0]
	v_cvt_pk_fp8_f32 v134, v32, v36
	v_cvt_pk_fp8_f32 v142, v33, v37
	v_cvt_pk_fp8_f32 v150, v34, v38
	v_cvt_pk_fp8_f32 v158, v35, v39
	v_cvt_pk_fp8_f32 v134, v40, v44 op_sel:[0,0,1]
	v_cvt_pk_fp8_f32 v142, v41, v45 op_sel:[0,0,1]
	v_cvt_pk_fp8_f32 v150, v42, v46 op_sel:[0,0,1]
	v_cvt_pk_fp8_f32 v158, v43, v47 op_sel:[0,0,1]
	s_waitcnt vmcnt(16)
	v_pk_mul_f32 v[48:49], v[48:49], s[16:17] op_sel_hi:[1,0]
	v_pk_mul_f32 v[50:51], v[50:51], s[16:17] op_sel_hi:[1,0]
	v_pk_mul_f32 v[52:53], v[52:53], s[16:17] op_sel_hi:[1,0]
	v_pk_mul_f32 v[54:55], v[54:55], s[16:17] op_sel_hi:[1,0]
	v_pk_mul_f32 v[56:57], v[56:57], s[16:17] op_sel_hi:[1,0]
	v_pk_mul_f32 v[58:59], v[58:59], s[16:17] op_sel_hi:[1,0]
	v_pk_mul_f32 v[60:61], v[60:61], s[16:17] op_sel_hi:[1,0]
	v_pk_mul_f32 v[62:63], v[62:63], s[16:17] op_sel_hi:[1,0]
	v_cvt_pk_fp8_f32 v135, v48, v52
	v_cvt_pk_fp8_f32 v143, v49, v53
	v_cvt_pk_fp8_f32 v151, v50, v54
	v_cvt_pk_fp8_f32 v159, v51, v55
	v_cvt_pk_fp8_f32 v135, v56, v60 op_sel:[0,0,1]
	v_cvt_pk_fp8_f32 v143, v57, v61 op_sel:[0,0,1]
	v_cvt_pk_fp8_f32 v151, v58, v62 op_sel:[0,0,1]
	v_cvt_pk_fp8_f32 v159, v59, v63 op_sel:[0,0,1]
	s_waitcnt vmcnt(12)
	v_pk_mul_f32 v[64:65], v[64:65], s[16:17] op_sel_hi:[1,0]
	v_pk_mul_f32 v[66:67], v[66:67], s[16:17] op_sel_hi:[1,0]
	v_pk_mul_f32 v[68:69], v[68:69], s[16:17] op_sel_hi:[1,0]
	v_pk_mul_f32 v[70:71], v[70:71], s[16:17] op_sel_hi:[1,0]
	v_pk_mul_f32 v[72:73], v[72:73], s[16:17] op_sel_hi:[1,0]
	v_pk_mul_f32 v[74:75], v[74:75], s[16:17] op_sel_hi:[1,0]
	v_pk_mul_f32 v[76:77], v[76:77], s[16:17] op_sel_hi:[1,0]
	v_pk_mul_f32 v[78:79], v[78:79], s[16:17] op_sel_hi:[1,0]
	v_cvt_pk_fp8_f32 v136, v64, v68
	v_cvt_pk_fp8_f32 v144, v65, v69
	v_cvt_pk_fp8_f32 v152, v66, v70
	v_cvt_pk_fp8_f32 v160, v67, v71
	v_cvt_pk_fp8_f32 v136, v72, v76 op_sel:[0,0,1]
	v_cvt_pk_fp8_f32 v144, v73, v77 op_sel:[0,0,1]
	v_cvt_pk_fp8_f32 v152, v74, v78 op_sel:[0,0,1]
	v_cvt_pk_fp8_f32 v160, v75, v79 op_sel:[0,0,1]
	s_waitcnt vmcnt(8)
	v_pk_mul_f32 v[80:81], v[80:81], s[16:17] op_sel_hi:[1,0]
	v_pk_mul_f32 v[82:83], v[82:83], s[16:17] op_sel_hi:[1,0]
	v_pk_mul_f32 v[84:85], v[84:85], s[16:17] op_sel_hi:[1,0]
	v_pk_mul_f32 v[86:87], v[86:87], s[16:17] op_sel_hi:[1,0]
	v_pk_mul_f32 v[88:89], v[88:89], s[16:17] op_sel_hi:[1,0]
	v_pk_mul_f32 v[90:91], v[90:91], s[16:17] op_sel_hi:[1,0]
	v_pk_mul_f32 v[92:93], v[92:93], s[16:17] op_sel_hi:[1,0]
	v_pk_mul_f32 v[94:95], v[94:95], s[16:17] op_sel_hi:[1,0]
	v_cvt_pk_fp8_f32 v137, v80, v84
	v_cvt_pk_fp8_f32 v145, v81, v85
	v_cvt_pk_fp8_f32 v153, v82, v86
	v_cvt_pk_fp8_f32 v161, v83, v87
	v_cvt_pk_fp8_f32 v137, v88, v92 op_sel:[0,0,1]
	v_cvt_pk_fp8_f32 v145, v89, v93 op_sel:[0,0,1]
	v_cvt_pk_fp8_f32 v153, v90, v94 op_sel:[0,0,1]
	v_cvt_pk_fp8_f32 v161, v91, v95 op_sel:[0,0,1]
	s_waitcnt vmcnt(4)
	v_pk_mul_f32 v[100:101], v[100:101], s[16:17] op_sel_hi:[1,0]
	v_pk_mul_f32 v[102:103], v[102:103], s[16:17] op_sel_hi:[1,0]
	v_pk_mul_f32 v[104:105], v[104:105], s[16:17] op_sel_hi:[1,0]
	v_pk_mul_f32 v[106:107], v[106:107], s[16:17] op_sel_hi:[1,0]
	v_pk_mul_f32 v[108:109], v[108:109], s[16:17] op_sel_hi:[1,0]
	v_pk_mul_f32 v[110:111], v[110:111], s[16:17] op_sel_hi:[1,0]
	v_pk_mul_f32 v[112:113], v[112:113], s[16:17] op_sel_hi:[1,0]
	v_pk_mul_f32 v[114:115], v[114:115], s[16:17] op_sel_hi:[1,0]
	v_cvt_pk_fp8_f32 v138, v100, v104
	v_cvt_pk_fp8_f32 v146, v101, v105
	v_cvt_pk_fp8_f32 v154, v102, v106
	v_cvt_pk_fp8_f32 v162, v103, v107
	v_cvt_pk_fp8_f32 v138, v108, v112 op_sel:[0,0,1]
	v_cvt_pk_fp8_f32 v146, v109, v113 op_sel:[0,0,1]
	v_cvt_pk_fp8_f32 v154, v110, v114 op_sel:[0,0,1]
	v_cvt_pk_fp8_f32 v162, v111, v115 op_sel:[0,0,1]
	s_waitcnt vmcnt(0)
	v_pk_mul_f32 v[116:117], v[116:117], s[16:17] op_sel_hi:[1,0]
	v_pk_mul_f32 v[118:119], v[118:119], s[16:17] op_sel_hi:[1,0]
	v_pk_mul_f32 v[120:121], v[120:121], s[16:17] op_sel_hi:[1,0]
	v_pk_mul_f32 v[122:123], v[122:123], s[16:17] op_sel_hi:[1,0]
	v_pk_mul_f32 v[124:125], v[124:125], s[16:17] op_sel_hi:[1,0]
	v_pk_mul_f32 v[126:127], v[126:127], s[16:17] op_sel_hi:[1,0]
	v_pk_mul_f32 v[128:129], v[128:129], s[16:17] op_sel_hi:[1,0]
	v_pk_mul_f32 v[130:131], v[130:131], s[16:17] op_sel_hi:[1,0]
	v_cvt_pk_fp8_f32 v139, v116, v120
	v_cvt_pk_fp8_f32 v147, v117, v121
	v_cvt_pk_fp8_f32 v155, v118, v122
	v_cvt_pk_fp8_f32 v163, v119, v123
	v_cvt_pk_fp8_f32 v139, v124, v128 op_sel:[0,0,1]
	v_cvt_pk_fp8_f32 v147, v125, v129 op_sel:[0,0,1]
	v_cvt_pk_fp8_f32 v155, v126, v130 op_sel:[0,0,1]
	v_cvt_pk_fp8_f32 v163, v127, v131 op_sel:[0,0,1]
	s_nop 0
	ds_write_b128 v165, v[132:135]
	ds_write_b128 v165, v[136:139] offset:16
	ds_write_b128 v165, v[140:143] offset:144
	ds_write_b128 v165, v[144:147] offset:160
	ds_write_b128 v165, v[148:151] offset:288
	ds_write_b128 v165, v[152:155] offset:304
	ds_write_b128 v165, v[156:159] offset:432
	ds_write_b128 v165, v[160:163] offset:448
	s_waitcnt lgkmcnt(0)
	ds_read_b128 v[0:3], v166
	ds_read_b128 v[4:7], v166 offset:1152
	ds_read_b128 v[8:11], v166 offset:2304
	ds_read_b128 v[12:15], v166 offset:3456
	ds_read_b128 v[16:19], v166 offset:4608
	ds_read_b128 v[20:23], v166 offset:5760
	ds_read_b128 v[24:27], v166 offset:6912
	ds_read_b128 v[28:31], v166 offset:8064
	s_waitcnt lgkmcnt(7)
	global_store_dwordx4 v167, v[0:3], s[12:13] nt
	s_add_u32 s12, s12, s15
	s_addc_u32 s13, s13, 0
	s_waitcnt lgkmcnt(6)
	global_store_dwordx4 v167, v[4:7], s[12:13] nt
	s_add_u32 s12, s12, s15
	s_addc_u32 s13, s13, 0
	s_waitcnt lgkmcnt(5)
	global_store_dwordx4 v167, v[8:11], s[12:13] nt
	s_add_u32 s12, s12, s15
	s_addc_u32 s13, s13, 0
	s_waitcnt lgkmcnt(4)
	global_store_dwordx4 v167, v[12:15], s[12:13] nt
	s_add_u32 s12, s12, s15
	s_addc_u32 s13, s13, 0
	s_waitcnt lgkmcnt(3)
	global_store_dwordx4 v167, v[16:19], s[12:13] nt
	s_add_u32 s12, s12, s15
	s_addc_u32 s13, s13, 0
	s_waitcnt lgkmcnt(2)
	global_store_dwordx4 v167, v[20:23], s[12:13] nt
	s_add_u32 s12, s12, s15
	s_addc_u32 s13, s13, 0
	s_waitcnt lgkmcnt(1)
	global_store_dwordx4 v167, v[24:27], s[12:13] nt
	s_add_u32 s12, s12, s15
	s_addc_u32 s13, s13, 0
	s_waitcnt lgkmcnt(0)
	global_store_dwordx4 v167, v[28:31], s[12:13] nt
	s_branch .LBB0_869
